# topk phase hand-rewritten: bitwise bisection with ballot counts and one barrier per step instead of LDS-atomic radix passes; on top of the gating rewrite
# baseline (speedup 1.0000x reference)
.Ltk_new:
	s_load_dwordx2 s[14:15], s[0:1], 0xa0
	s_mov_b32 s16, s88
	v_lshlrev_b32_e32 v26, 5, v0
	v_lshrrev_b32_e32 v42, 6, v0
	v_mov_b32_e32 v28, 0
	v_lshlrev_b32_e32 v27, 2, v42
	v_readfirstlane_b32 s23, v42
	s_waitcnt lgkmcnt(0)
.Ltk_prob:
	s_lshr_b32 s17, s16, 4
	s_and_b32 s18, s16, 15
	s_lshl_b32 s4, s16, 14
	s_add_u32 s24, s14, 0x37900000
	s_addc_u32 s25, s15, 0
	s_add_u32 s24, s24, s4
	s_addc_u32 s25, s25, 0
	global_load_dwordx4 v[2:5], v26, s[24:25]
	global_load_dwordx4 v[6:9], v26, s[24:25] offset:16
	s_lshl_b32 s4, s17, 14
	s_add_u32 s26, s14, 0x37dc0000
	s_addc_u32 s27, s15, 0
	s_add_u32 s26, s26, s4
	s_addc_u32 s27, s27, 0
	global_load_dwordx4 v[10:13], v26, s[26:27]
	global_load_dwordx4 v[14:17], v26, s[26:27] offset:16
	s_mov_b32 s5, 0
	s_brev_b32 s6, 1
	s_movk_i32 s13, 16
	s_waitcnt vmcnt(2)
.Ltk_bis:
	s_or_b32 s8, s5, s6
	s_mov_b32 s9, 0
	v_cmp_le_u32_e64 s[28:29], s8, v2
	v_cmp_le_u32_e64 s[30:31], s8, v3
	v_cmp_le_u32_e64 s[34:35], s8, v4
	v_cmp_le_u32_e64 s[36:37], s8, v5
	s_bcnt1_i32_b64 s12, s[28:29]
	s_add_i32 s9, s9, s12
	s_bcnt1_i32_b64 s12, s[30:31]
	s_add_i32 s9, s9, s12
	s_bcnt1_i32_b64 s12, s[34:35]
	s_add_i32 s9, s9, s12
	s_bcnt1_i32_b64 s12, s[36:37]
	s_add_i32 s9, s9, s12
	v_cmp_le_u32_e64 s[28:29], s8, v6
	v_cmp_le_u32_e64 s[30:31], s8, v7
	v_cmp_le_u32_e64 s[34:35], s8, v8
	v_cmp_le_u32_e64 s[36:37], s8, v9
	s_bcnt1_i32_b64 s12, s[28:29]
	s_add_i32 s9, s9, s12
	s_bcnt1_i32_b64 s12, s[30:31]
	s_add_i32 s9, s9, s12
	s_bcnt1_i32_b64 s12, s[34:35]
	s_add_i32 s9, s9, s12
	s_bcnt1_i32_b64 s12, s[36:37]
	s_add_i32 s9, s9, s12
	v_mov_b32_e32 v29, s9
	ds_write_b32 v27, v29 offset:0
	s_waitcnt lgkmcnt(0)
	s_barrier
	ds_read_b128 v[32:35], v28 offset:0
	ds_read_b128 v[36:39], v28 offset:16
	s_waitcnt lgkmcnt(0)
	v_add_u32_e32 v32, v32, v33
	v_add_u32_e32 v34, v34, v35
	v_add_u32_e32 v36, v36, v37
	v_add_u32_e32 v38, v38, v39
	v_add_u32_e32 v32, v32, v34
	v_add_u32_e32 v36, v36, v38
	v_add_u32_e32 v32, v32, v36
	s_nop 0
	v_readfirstlane_b32 s9, v32
	s_cmp_ge_u32 s9, 0x200
	s_cselect_b32 s5, s8, s5
	s_lshr_b32 s6, s6, 1
	s_or_b32 s8, s5, s6
	s_mov_b32 s9, 0
	v_cmp_le_u32_e64 s[28:29], s8, v2
	v_cmp_le_u32_e64 s[30:31], s8, v3
	v_cmp_le_u32_e64 s[34:35], s8, v4
	v_cmp_le_u32_e64 s[36:37], s8, v5
	s_bcnt1_i32_b64 s12, s[28:29]
	s_add_i32 s9, s9, s12
	s_bcnt1_i32_b64 s12, s[30:31]
	s_add_i32 s9, s9, s12
	s_bcnt1_i32_b64 s12, s[34:35]
	s_add_i32 s9, s9, s12
	s_bcnt1_i32_b64 s12, s[36:37]
	s_add_i32 s9, s9, s12
	v_cmp_le_u32_e64 s[28:29], s8, v6
	v_cmp_le_u32_e64 s[30:31], s8, v7
	v_cmp_le_u32_e64 s[34:35], s8, v8
	v_cmp_le_u32_e64 s[36:37], s8, v9
	s_bcnt1_i32_b64 s12, s[28:29]
	s_add_i32 s9, s9, s12
	s_bcnt1_i32_b64 s12, s[30:31]
	s_add_i32 s9, s9, s12
	s_bcnt1_i32_b64 s12, s[34:35]
	s_add_i32 s9, s9, s12
	s_bcnt1_i32_b64 s12, s[36:37]
	s_add_i32 s9, s9, s12
	v_mov_b32_e32 v29, s9
	ds_write_b32 v27, v29 offset:32
	s_waitcnt lgkmcnt(0)
	s_barrier
	ds_read_b128 v[32:35], v28 offset:32
	ds_read_b128 v[36:39], v28 offset:48
	s_waitcnt lgkmcnt(0)
	v_add_u32_e32 v32, v32, v33
	v_add_u32_e32 v34, v34, v35
	v_add_u32_e32 v36, v36, v37
	v_add_u32_e32 v38, v38, v39
	v_add_u32_e32 v32, v32, v34
	v_add_u32_e32 v36, v36, v38
	v_add_u32_e32 v32, v32, v36
	s_nop 0
	v_readfirstlane_b32 s9, v32
	s_cmp_ge_u32 s9, 0x200
	s_cselect_b32 s5, s8, s5
	s_lshr_b32 s6, s6, 1
	s_add_i32 s13, s13, -1
	s_cmp_lg_u32 s13, 0
	s_cbranch_scc1 .Ltk_bis
	s_mov_b32 s9, 0
	s_mov_b32 s12, 0
	v_mov_b32_e32 v40, 0
	v_mov_b32_e32 v41, 0
	v_cmp_lt_u32_e64 s[28:29], s5, v2
	v_cmp_eq_u32_e64 s[30:31], s5, v2
	s_bcnt1_i32_b64 s8, s[28:29]
	s_add_i32 s9, s9, s8
	s_bcnt1_i32_b64 s8, s[30:31]
	s_add_i32 s12, s12, s8
	v_mbcnt_lo_u32_b32 v40, s28, v40
	v_mbcnt_hi_u32_b32 v40, s29, v40
	v_mbcnt_lo_u32_b32 v41, s30, v41
	v_mbcnt_hi_u32_b32 v41, s31, v41
	v_cmp_lt_u32_e64 s[28:29], s5, v3
	v_cmp_eq_u32_e64 s[30:31], s5, v3
	s_bcnt1_i32_b64 s8, s[28:29]
	s_add_i32 s9, s9, s8
	s_bcnt1_i32_b64 s8, s[30:31]
	s_add_i32 s12, s12, s8
	v_mbcnt_lo_u32_b32 v40, s28, v40
	v_mbcnt_hi_u32_b32 v40, s29, v40
	v_mbcnt_lo_u32_b32 v41, s30, v41
	v_mbcnt_hi_u32_b32 v41, s31, v41
	v_cmp_lt_u32_e64 s[28:29], s5, v4
	v_cmp_eq_u32_e64 s[30:31], s5, v4
	s_bcnt1_i32_b64 s8, s[28:29]
	s_add_i32 s9, s9, s8
	s_bcnt1_i32_b64 s8, s[30:31]
	s_add_i32 s12, s12, s8
	v_mbcnt_lo_u32_b32 v40, s28, v40
	v_mbcnt_hi_u32_b32 v40, s29, v40
	v_mbcnt_lo_u32_b32 v41, s30, v41
	v_mbcnt_hi_u32_b32 v41, s31, v41
	v_cmp_lt_u32_e64 s[28:29], s5, v5
	v_cmp_eq_u32_e64 s[30:31], s5, v5
	s_bcnt1_i32_b64 s8, s[28:29]
	s_add_i32 s9, s9, s8
	s_bcnt1_i32_b64 s8, s[30:31]
	s_add_i32 s12, s12, s8
	v_mbcnt_lo_u32_b32 v40, s28, v40
	v_mbcnt_hi_u32_b32 v40, s29, v40
	v_mbcnt_lo_u32_b32 v41, s30, v41
	v_mbcnt_hi_u32_b32 v41, s31, v41
	v_cmp_lt_u32_e64 s[28:29], s5, v6
	v_cmp_eq_u32_e64 s[30:31], s5, v6
	s_bcnt1_i32_b64 s8, s[28:29]
	s_add_i32 s9, s9, s8
	s_bcnt1_i32_b64 s8, s[30:31]
	s_add_i32 s12, s12, s8
	v_mbcnt_lo_u32_b32 v40, s28, v40
	v_mbcnt_hi_u32_b32 v40, s29, v40
	v_mbcnt_lo_u32_b32 v41, s30, v41
	v_mbcnt_hi_u32_b32 v41, s31, v41
	v_cmp_lt_u32_e64 s[28:29], s5, v7
	v_cmp_eq_u32_e64 s[30:31], s5, v7
	s_bcnt1_i32_b64 s8, s[28:29]
	s_add_i32 s9, s9, s8
	s_bcnt1_i32_b64 s8, s[30:31]
	s_add_i32 s12, s12, s8
	v_mbcnt_lo_u32_b32 v40, s28, v40
	v_mbcnt_hi_u32_b32 v40, s29, v40
	v_mbcnt_lo_u32_b32 v41, s30, v41
	v_mbcnt_hi_u32_b32 v41, s31, v41
	v_cmp_lt_u32_e64 s[28:29], s5, v8
	v_cmp_eq_u32_e64 s[30:31], s5, v8
	s_bcnt1_i32_b64 s8, s[28:29]
	s_add_i32 s9, s9, s8
	s_bcnt1_i32_b64 s8, s[30:31]
	s_add_i32 s12, s12, s8
	v_mbcnt_lo_u32_b32 v40, s28, v40
	v_mbcnt_hi_u32_b32 v40, s29, v40
	v_mbcnt_lo_u32_b32 v41, s30, v41
	v_mbcnt_hi_u32_b32 v41, s31, v41
	v_cmp_lt_u32_e64 s[28:29], s5, v9
	v_cmp_eq_u32_e64 s[30:31], s5, v9
	s_bcnt1_i32_b64 s8, s[28:29]
	s_add_i32 s9, s9, s8
	s_bcnt1_i32_b64 s8, s[30:31]
	s_add_i32 s12, s12, s8
	v_mbcnt_lo_u32_b32 v40, s28, v40
	v_mbcnt_hi_u32_b32 v40, s29, v40
	v_mbcnt_lo_u32_b32 v41, s30, v41
	v_mbcnt_hi_u32_b32 v41, s31, v41
	s_lshl_b32 s12, s12, 16
	s_or_b32 s9, s9, s12
	v_mov_b32_e32 v29, s9
	ds_write_b32 v27, v29 offset:64
	s_waitcnt lgkmcnt(0)
	s_barrier
	ds_read_b128 v[32:35], v28 offset:64
	ds_read_b128 v[36:39], v28 offset:80
	s_waitcnt lgkmcnt(0)
	s_mov_b32 s4, 0
	s_mov_b32 s7, 0
	v_readfirstlane_b32 s8, v32
	s_add_i32 s7, s7, s8
	s_cmp_lt_u32 0, s23
	s_cselect_b32 s8, s8, 0
	s_add_i32 s4, s4, s8
	v_readfirstlane_b32 s8, v33
	s_add_i32 s7, s7, s8
	s_cmp_lt_u32 1, s23
	s_cselect_b32 s8, s8, 0
	s_add_i32 s4, s4, s8
	v_readfirstlane_b32 s8, v34
	s_add_i32 s7, s7, s8
	s_cmp_lt_u32 2, s23
	s_cselect_b32 s8, s8, 0
	s_add_i32 s4, s4, s8
	v_readfirstlane_b32 s8, v35
	s_add_i32 s7, s7, s8
	s_cmp_lt_u32 3, s23
	s_cselect_b32 s8, s8, 0
	s_add_i32 s4, s4, s8
	v_readfirstlane_b32 s8, v36
	s_add_i32 s7, s7, s8
	s_cmp_lt_u32 4, s23
	s_cselect_b32 s8, s8, 0
	s_add_i32 s4, s4, s8
	v_readfirstlane_b32 s8, v37
	s_add_i32 s7, s7, s8
	s_cmp_lt_u32 5, s23
	s_cselect_b32 s8, s8, 0
	s_add_i32 s4, s4, s8
	v_readfirstlane_b32 s8, v38
	s_add_i32 s7, s7, s8
	s_cmp_lt_u32 6, s23
	s_cselect_b32 s8, s8, 0
	s_add_i32 s4, s4, s8
	v_readfirstlane_b32 s8, v39
	s_add_i32 s7, s7, s8
	s_cmp_lt_u32 7, s23
	s_cselect_b32 s8, s8, 0
	s_add_i32 s4, s4, s8
	s_and_b32 s12, s7, 0xffff
	s_sub_i32 s13, 0x200, s12
	s_and_b32 s8, s4, 0xffff
	s_lshr_b32 s9, s4, 16
	v_add_u32_e32 v40, s8, v40
	v_add_u32_e32 v41, s9, v41
	s_lshl_b32 s4, s18, 3
	s_add_i32 s4, s4, s17
	s_lshl_b32 s4, s4, 9
	s_lshl_b32 s6, s17, 12
	v_lshl_add_u32 v46, v0, 3, s6
	s_add_u32 s36, s14, 0x37d00000
	s_addc_u32 s37, s15, 0
	s_add_u32 s38, s14, 0x37d80000
	s_addc_u32 s39, s15, 0
	s_add_u32 s40, s14, 0x37d40000
	s_addc_u32 s41, s15, 0
	s_waitcnt vmcnt(0)
	v_cmp_lt_u32_e64 s[28:29], s5, v2
	v_cmp_eq_u32_e64 s[30:31], s5, v2
	v_cmp_gt_u32_e64 s[34:35], s13, v41
	v_min_u32_e32 v42, s13, v41
	v_add_u32_e32 v43, v40, v41
	v_add_u32_e32 v42, v42, v40
	s_and_b64 s[34:35], s[34:35], s[30:31]
	s_or_b64 s[42:43], s[34:35], s[28:29]
	v_cndmask_b32_e64 v42, v43, v42, s[28:29]
	v_add_u32_e32 v42, s4, v42
	v_cndmask_b32_e64 v44, 0, 1, s[28:29]
	v_cndmask_b32_e64 v45, 0, 1, s[30:31]
	v_cndmask_b32_e64 v18, -1, v42, s[42:43]
	v_add_u32_e32 v40, v40, v44
	v_add_u32_e32 v41, v41, v45
	v_lshlrev_b32_e32 v47, 2, v42
	s_and_saveexec_b64 s[44:45], s[42:43]
	global_store_dword v47, v46, s[36:37]
	global_store_dword v47, v2, s[38:39]
	global_store_dword v47, v10, s[40:41]
	s_mov_b64 exec, s[44:45]
	v_cmp_lt_u32_e64 s[28:29], s5, v3
	v_cmp_eq_u32_e64 s[30:31], s5, v3
	v_cmp_gt_u32_e64 s[34:35], s13, v41
	v_min_u32_e32 v42, s13, v41
	v_add_u32_e32 v43, v40, v41
	v_add_u32_e32 v42, v42, v40
	s_and_b64 s[34:35], s[34:35], s[30:31]
	s_or_b64 s[42:43], s[34:35], s[28:29]
	v_cndmask_b32_e64 v42, v43, v42, s[28:29]
	v_add_u32_e32 v42, s4, v42
	v_cndmask_b32_e64 v44, 0, 1, s[28:29]
	v_cndmask_b32_e64 v45, 0, 1, s[30:31]
	v_cndmask_b32_e64 v19, -1, v42, s[42:43]
	v_add_u32_e32 v40, v40, v44
	v_add_u32_e32 v41, v41, v45
	v_lshlrev_b32_e32 v47, 2, v42
	v_add_u32_e32 v46, 1, v46
	s_and_saveexec_b64 s[44:45], s[42:43]
	global_store_dword v47, v46, s[36:37]
	global_store_dword v47, v3, s[38:39]
	global_store_dword v47, v11, s[40:41]
	s_mov_b64 exec, s[44:45]
	v_cmp_lt_u32_e64 s[28:29], s5, v4
	v_cmp_eq_u32_e64 s[30:31], s5, v4
	v_cmp_gt_u32_e64 s[34:35], s13, v41
	v_min_u32_e32 v42, s13, v41
	v_add_u32_e32 v43, v40, v41
	v_add_u32_e32 v42, v42, v40
	s_and_b64 s[34:35], s[34:35], s[30:31]
	s_or_b64 s[42:43], s[34:35], s[28:29]
	v_cndmask_b32_e64 v42, v43, v42, s[28:29]
	v_add_u32_e32 v42, s4, v42
	v_cndmask_b32_e64 v44, 0, 1, s[28:29]
	v_cndmask_b32_e64 v45, 0, 1, s[30:31]
	v_cndmask_b32_e64 v20, -1, v42, s[42:43]
	v_add_u32_e32 v40, v40, v44
	v_add_u32_e32 v41, v41, v45
	v_lshlrev_b32_e32 v47, 2, v42
	v_add_u32_e32 v46, 1, v46
	s_and_saveexec_b64 s[44:45], s[42:43]
	global_store_dword v47, v46, s[36:37]
	global_store_dword v47, v4, s[38:39]
	global_store_dword v47, v12, s[40:41]
	s_mov_b64 exec, s[44:45]
	v_cmp_lt_u32_e64 s[28:29], s5, v5
	v_cmp_eq_u32_e64 s[30:31], s5, v5
	v_cmp_gt_u32_e64 s[34:35], s13, v41
	v_min_u32_e32 v42, s13, v41
	v_add_u32_e32 v43, v40, v41
	v_add_u32_e32 v42, v42, v40
	s_and_b64 s[34:35], s[34:35], s[30:31]
	s_or_b64 s[42:43], s[34:35], s[28:29]
	v_cndmask_b32_e64 v42, v43, v42, s[28:29]
	v_add_u32_e32 v42, s4, v42
	v_cndmask_b32_e64 v44, 0, 1, s[28:29]
	v_cndmask_b32_e64 v45, 0, 1, s[30:31]
	v_cndmask_b32_e64 v21, -1, v42, s[42:43]
	v_add_u32_e32 v40, v40, v44
	v_add_u32_e32 v41, v41, v45
	v_lshlrev_b32_e32 v47, 2, v42
	v_add_u32_e32 v46, 1, v46
	s_and_saveexec_b64 s[44:45], s[42:43]
	global_store_dword v47, v46, s[36:37]
	global_store_dword v47, v5, s[38:39]
	global_store_dword v47, v13, s[40:41]
	s_mov_b64 exec, s[44:45]
	v_cmp_lt_u32_e64 s[28:29], s5, v6
	v_cmp_eq_u32_e64 s[30:31], s5, v6
	v_cmp_gt_u32_e64 s[34:35], s13, v41
	v_min_u32_e32 v42, s13, v41
	v_add_u32_e32 v43, v40, v41
	v_add_u32_e32 v42, v42, v40
	s_and_b64 s[34:35], s[34:35], s[30:31]
	s_or_b64 s[42:43], s[34:35], s[28:29]
	v_cndmask_b32_e64 v42, v43, v42, s[28:29]
	v_add_u32_e32 v42, s4, v42
	v_cndmask_b32_e64 v44, 0, 1, s[28:29]
	v_cndmask_b32_e64 v45, 0, 1, s[30:31]
	v_cndmask_b32_e64 v22, -1, v42, s[42:43]
	v_add_u32_e32 v40, v40, v44
	v_add_u32_e32 v41, v41, v45
	v_lshlrev_b32_e32 v47, 2, v42
	v_add_u32_e32 v46, 1, v46
	s_and_saveexec_b64 s[44:45], s[42:43]
	global_store_dword v47, v46, s[36:37]
	global_store_dword v47, v6, s[38:39]
	global_store_dword v47, v14, s[40:41]
	s_mov_b64 exec, s[44:45]
	v_cmp_lt_u32_e64 s[28:29], s5, v7
	v_cmp_eq_u32_e64 s[30:31], s5, v7
	v_cmp_gt_u32_e64 s[34:35], s13, v41
	v_min_u32_e32 v42, s13, v41
	v_add_u32_e32 v43, v40, v41
	v_add_u32_e32 v42, v42, v40
	s_and_b64 s[34:35], s[34:35], s[30:31]
	s_or_b64 s[42:43], s[34:35], s[28:29]
	v_cndmask_b32_e64 v42, v43, v42, s[28:29]
	v_add_u32_e32 v42, s4, v42
	v_cndmask_b32_e64 v44, 0, 1, s[28:29]
	v_cndmask_b32_e64 v45, 0, 1, s[30:31]
	v_cndmask_b32_e64 v23, -1, v42, s[42:43]
	v_add_u32_e32 v40, v40, v44
	v_add_u32_e32 v41, v41, v45
	v_lshlrev_b32_e32 v47, 2, v42
	v_add_u32_e32 v46, 1, v46
	s_and_saveexec_b64 s[44:45], s[42:43]
	global_store_dword v47, v46, s[36:37]
	global_store_dword v47, v7, s[38:39]
	global_store_dword v47, v15, s[40:41]
	s_mov_b64 exec, s[44:45]
	v_cmp_lt_u32_e64 s[28:29], s5, v8
	v_cmp_eq_u32_e64 s[30:31], s5, v8
	v_cmp_gt_u32_e64 s[34:35], s13, v41
	v_min_u32_e32 v42, s13, v41
	v_add_u32_e32 v43, v40, v41
	v_add_u32_e32 v42, v42, v40
	s_and_b64 s[34:35], s[34:35], s[30:31]
	s_or_b64 s[42:43], s[34:35], s[28:29]
	v_cndmask_b32_e64 v42, v43, v42, s[28:29]
	v_add_u32_e32 v42, s4, v42
	v_cndmask_b32_e64 v44, 0, 1, s[28:29]
	v_cndmask_b32_e64 v45, 0, 1, s[30:31]
	v_cndmask_b32_e64 v24, -1, v42, s[42:43]
	v_add_u32_e32 v40, v40, v44
	v_add_u32_e32 v41, v41, v45
	v_lshlrev_b32_e32 v47, 2, v42
	v_add_u32_e32 v46, 1, v46
	s_and_saveexec_b64 s[44:45], s[42:43]
	global_store_dword v47, v46, s[36:37]
	global_store_dword v47, v8, s[38:39]
	global_store_dword v47, v16, s[40:41]
	s_mov_b64 exec, s[44:45]
	v_cmp_lt_u32_e64 s[28:29], s5, v9
	v_cmp_eq_u32_e64 s[30:31], s5, v9
	v_cmp_gt_u32_e64 s[34:35], s13, v41
	v_min_u32_e32 v42, s13, v41
	v_add_u32_e32 v43, v40, v41
	v_add_u32_e32 v42, v42, v40
	s_and_b64 s[34:35], s[34:35], s[30:31]
	s_or_b64 s[42:43], s[34:35], s[28:29]
	v_cndmask_b32_e64 v42, v43, v42, s[28:29]
	v_add_u32_e32 v42, s4, v42
	v_cndmask_b32_e64 v44, 0, 1, s[28:29]
	v_cndmask_b32_e64 v45, 0, 1, s[30:31]
	v_cndmask_b32_e64 v25, -1, v42, s[42:43]
	v_add_u32_e32 v40, v40, v44
	v_add_u32_e32 v41, v41, v45
	v_lshlrev_b32_e32 v47, 2, v42
	v_add_u32_e32 v46, 1, v46
	s_and_saveexec_b64 s[44:45], s[42:43]
	global_store_dword v47, v46, s[36:37]
	global_store_dword v47, v9, s[38:39]
	global_store_dword v47, v17, s[40:41]
	s_mov_b64 exec, s[44:45]
	s_lshl_b32 s4, s16, 14
	s_add_u32 s24, s14, 0x37b00000
	s_addc_u32 s25, s15, 0
	s_add_u32 s24, s24, s4
	s_addc_u32 s25, s25, 0
	global_store_dwordx4 v26, v[18:21], s[24:25]
	global_store_dwordx4 v26, v[22:25], s[24:25] offset:16
	s_add_i32 s16, s16, s96
	s_cmpk_lt_u32 s16, 0x80
	s_cbranch_scc0 .LBB0_1167
	s_barrier
	s_branch .Ltk_prob
